# v25 + hand-written software-pipelined dilated-attention combine loop (all loads of a row issued together two rows ahead, gains loaded once)
# speedup vs baseline: 1.0271x; 1.0010x over previous
.LBB0_380:
	v_readlane_b32 s4, v253, 4
	v_readlane_b32 s5, v253, 5
	s_andn2_b64 vcc, exec, s[4:5]
	s_nop 0
	v_cndmask_b32_e64 v0, 0, 1, s[4:5]
	v_cmp_ne_u32_e64 s[10:11], 1, v0
	s_cbranch_vccnz .LBB0_383
	v_readlane_b32 s40, v255, 5
	v_readlane_b32 s41, v255, 6
	v_readlane_b32 s4, v255, 29
	v_readlane_b32 s5, v255, 30
	v_mbcnt_lo_u32_b32 v0, -1, 0
	v_mbcnt_hi_u32_b32 v0, -1, v0
	s_nop 4
	s_load_dwordx2 s[34:35], s[40:41], 0x128
	s_load_dwordx2 s[6:7], s[4:5], 0x60
	s_lshr_b32 s8, s95, 6
	s_lshl_b32 s9, s2, 3
	s_add_i32 s8, s8, s9
	v_and_b32_e32 v70, 7, v0
	v_lshlrev_b32_e32 v70, 6, v70
	v_lshlrev_b32_e32 v236, 5, v0
	s_lshl_b32 s9, s8, 11
	v_add_u32_e32 v1, s9, v236
	v_add_u32_e32 v1, 0x58200000, v1
	s_lshl_b32 s9, s8, 12
	v_add_u32_e32 v5, s9, v236
	v_add_u32_e32 v5, 0x36400800, v5
	v_lshrrev_b32_e32 v237, 3, v0
	v_lshlrev_b32_e32 v237, 2, v237
	s_lshl_b32 s9, s8, 5
	v_add_u32_e32 v2, s9, v237
	v_add_u32_e32 v2, 0x64200000, v2
	v_mov_b32_e32 v47, 0x358637bd
	s_waitcnt lgkmcnt(0)
	global_load_dwordx4 v[52:55], v70, s[6:7]
	global_load_dwordx4 v[56:59], v70, s[6:7] offset:16
	global_load_dwordx4 v[60:63], v70, s[6:7] offset:32
	global_load_dwordx4 v[64:67], v70, s[6:7] offset:48
	s_waitcnt vmcnt(0)
	global_load_dwordx4 v[20:23], v1, s[34:35] nt
	global_load_dwordx4 v[24:27], v1, s[34:35] offset:16 nt
	v_add_u32_e32 v236, 0x2000000, v1
	global_load_dword v44, v2, s[34:35]
	global_load_dwordx4 v[28:31], v236, s[34:35] nt
	global_load_dwordx4 v[32:35], v236, s[34:35] offset:16 nt
	v_add_u32_e32 v237, 0x4000000, v1
	v_add_u32_e32 v238, 0x80000, v2
	global_load_dword v45, v238, s[34:35]
	global_load_dwordx4 v[36:39], v237, s[34:35] nt
	global_load_dwordx4 v[40:43], v237, s[34:35] offset:16 nt
	v_add_u32_e32 v238, 0x100000, v2
	global_load_dword v46, v238, s[34:35]
	v_add_u32_e32 v1, 0x400000, v1
	v_add_u32_e32 v2, 0x10000, v2
	global_load_dwordx4 v[148:151], v1, s[34:35] nt
	global_load_dwordx4 v[152:155], v1, s[34:35] offset:16 nt
	v_add_u32_e32 v236, 0x2000000, v1
	global_load_dword v172, v2, s[34:35]
	global_load_dwordx4 v[156:159], v236, s[34:35] nt
	global_load_dwordx4 v[160:163], v236, s[34:35] offset:16 nt
	v_add_u32_e32 v237, 0x4000000, v1
	v_add_u32_e32 v238, 0x80000, v2
	global_load_dword v173, v238, s[34:35]
	global_load_dwordx4 v[164:167], v237, s[34:35] nt
	global_load_dwordx4 v[168:171], v237, s[34:35] offset:16 nt
	v_add_u32_e32 v238, 0x100000, v2
	global_load_dword v174, v238, s[34:35]
	v_add_u32_e32 v1, 0x400000, v1
	v_add_u32_e32 v2, 0x10000, v2
	s_mov_b32 s8, 0
	s_waitcnt vmcnt(9)
.Lcb_loop:
	s_waitcnt vmcnt(11)
	v_lshlrev_b32_e32 v220, 16, v20
	v_and_b32_e32 v221, 0xffff0000, v20
	v_lshlrev_b32_e32 v240, 16, v28
	v_and_b32_e32 v241, 0xffff0000, v28
	v_pk_add_f32 v[220:221], v[220:221], v[240:241]
	v_lshlrev_b32_e32 v240, 16, v36
	v_and_b32_e32 v241, 0xffff0000, v36
	v_pk_add_f32 v[220:221], v[220:221], v[240:241]
	v_lshlrev_b32_e32 v222, 16, v21
	v_and_b32_e32 v223, 0xffff0000, v21
	v_lshlrev_b32_e32 v240, 16, v29
	v_and_b32_e32 v241, 0xffff0000, v29
	v_pk_add_f32 v[222:223], v[222:223], v[240:241]
	v_lshlrev_b32_e32 v240, 16, v37
	v_and_b32_e32 v241, 0xffff0000, v37
	v_pk_add_f32 v[222:223], v[222:223], v[240:241]
	v_lshlrev_b32_e32 v224, 16, v22
	v_and_b32_e32 v225, 0xffff0000, v22
	v_lshlrev_b32_e32 v240, 16, v30
	v_and_b32_e32 v241, 0xffff0000, v30
	v_pk_add_f32 v[224:225], v[224:225], v[240:241]
	v_lshlrev_b32_e32 v240, 16, v38
	v_and_b32_e32 v241, 0xffff0000, v38
	v_pk_add_f32 v[224:225], v[224:225], v[240:241]
	v_lshlrev_b32_e32 v226, 16, v23
	v_and_b32_e32 v227, 0xffff0000, v23
	v_lshlrev_b32_e32 v240, 16, v31
	v_and_b32_e32 v241, 0xffff0000, v31
	v_pk_add_f32 v[226:227], v[226:227], v[240:241]
	v_lshlrev_b32_e32 v240, 16, v39
	v_and_b32_e32 v241, 0xffff0000, v39
	v_pk_add_f32 v[226:227], v[226:227], v[240:241]
	v_lshlrev_b32_e32 v228, 16, v24
	v_and_b32_e32 v229, 0xffff0000, v24
	v_lshlrev_b32_e32 v240, 16, v32
	v_and_b32_e32 v241, 0xffff0000, v32
	v_pk_add_f32 v[228:229], v[228:229], v[240:241]
	v_lshlrev_b32_e32 v240, 16, v40
	v_and_b32_e32 v241, 0xffff0000, v40
	v_pk_add_f32 v[228:229], v[228:229], v[240:241]
	v_lshlrev_b32_e32 v230, 16, v25
	v_and_b32_e32 v231, 0xffff0000, v25
	v_lshlrev_b32_e32 v240, 16, v33
	v_and_b32_e32 v241, 0xffff0000, v33
	v_pk_add_f32 v[230:231], v[230:231], v[240:241]
	v_lshlrev_b32_e32 v240, 16, v41
	v_and_b32_e32 v241, 0xffff0000, v41
	v_pk_add_f32 v[230:231], v[230:231], v[240:241]
	v_lshlrev_b32_e32 v232, 16, v26
	v_and_b32_e32 v233, 0xffff0000, v26
	v_lshlrev_b32_e32 v240, 16, v34
	v_and_b32_e32 v241, 0xffff0000, v34
	v_pk_add_f32 v[232:233], v[232:233], v[240:241]
	v_lshlrev_b32_e32 v240, 16, v42
	v_and_b32_e32 v241, 0xffff0000, v42
	v_pk_add_f32 v[232:233], v[232:233], v[240:241]
	v_lshlrev_b32_e32 v234, 16, v27
	v_and_b32_e32 v235, 0xffff0000, v27
	v_lshlrev_b32_e32 v240, 16, v35
	v_and_b32_e32 v241, 0xffff0000, v35
	v_pk_add_f32 v[234:235], v[234:235], v[240:241]
	v_lshlrev_b32_e32 v240, 16, v43
	v_and_b32_e32 v241, 0xffff0000, v43
	v_pk_add_f32 v[234:235], v[234:235], v[240:241]
	v_add_f32_e32 v247, v44, v45
	v_add_f32_e32 v247, v247, v46
	v_div_scale_f32 v239, s[12:13], v247, v247, 1.0
	v_rcp_f32_e32 v240, v239
	s_nop 0
	v_fma_f32 v241, -v239, v240, 1.0
	v_fmac_f32_e32 v240, v241, v240
	v_div_scale_f32 v244, vcc, 1.0, v247, 1.0
	v_mul_f32_e32 v245, v244, v240
	v_fma_f32 v246, -v239, v245, v244
	v_fmac_f32_e32 v245, v246, v240
	v_fma_f32 v239, -v239, v245, v244
	v_div_fmas_f32 v239, v239, v240, v245
	v_div_fixup_f32 v247, v239, v247, 1.0
	v_mul_f32_e32 v220, v247, v220
	v_mul_f32_e32 v221, v247, v221
	v_mul_f32_e32 v222, v247, v222
	v_mul_f32_e32 v223, v247, v223
	v_mul_f32_e32 v224, v247, v224
	v_mul_f32_e32 v225, v247, v225
	v_mul_f32_e32 v226, v247, v226
	v_mul_f32_e32 v227, v247, v227
	v_mul_f32_e32 v228, v247, v228
	v_mul_f32_e32 v229, v247, v229
	v_mul_f32_e32 v230, v247, v230
	v_mul_f32_e32 v231, v247, v231
	v_mul_f32_e32 v232, v247, v232
	v_mul_f32_e32 v233, v247, v233
	v_mul_f32_e32 v234, v247, v234
	v_mul_f32_e32 v235, v247, v235
	v_mul_f32_e32 v48, v220, v220
	v_fmac_f32_e32 v48, v221, v221
	v_mul_f32_e32 v49, v222, v222
	v_fmac_f32_e32 v49, v223, v223
	v_add_f32_e32 v48, v48, v49
	v_mov_b32_e32 v207, v48
	v_mul_f32_e32 v48, v224, v224
	v_fmac_f32_e32 v48, v225, v225
	v_mul_f32_e32 v49, v226, v226
	v_fmac_f32_e32 v49, v227, v227
	v_add_f32_e32 v48, v48, v49
	v_add_f32_e32 v207, v207, v48
	v_mul_f32_e32 v48, v228, v228
	v_fmac_f32_e32 v48, v229, v229
	v_mul_f32_e32 v49, v230, v230
	v_fmac_f32_e32 v49, v231, v231
	v_add_f32_e32 v48, v48, v49
	v_add_f32_e32 v207, v207, v48
	v_mul_f32_e32 v48, v232, v232
	v_fmac_f32_e32 v48, v233, v233
	v_mul_f32_e32 v49, v234, v234
	v_fmac_f32_e32 v49, v235, v235
	v_add_f32_e32 v48, v48, v49
	v_add_f32_e32 v207, v207, v48
	ds_swizzle_b32 v48, v207 offset:0x41f
	s_waitcnt lgkmcnt(0)
	v_add_f32_e32 v207, v207, v48
	ds_swizzle_b32 v48, v207 offset:0x81f
	s_waitcnt lgkmcnt(0)
	v_add_f32_e32 v207, v207, v48
	ds_swizzle_b32 v48, v207 offset:0x101f
	s_waitcnt lgkmcnt(0)
	v_add_f32_e32 v207, v207, v48
	v_fmamk_f32 v50, v207, 0x3c000000, v47
	v_sqrt_f32_e32 v51, v50
	s_nop 0
	v_add_u32_e32 v175, -1, v51
	v_fma_f32 v177, -v175, v51, v50
	v_cmp_ge_f32_e64 s[12:13], 0, v177
	v_add_u32_e32 v176, 1, v51
	s_nop 1
	v_cndmask_b32_e64 v175, v51, v175, s[12:13]
	v_fma_f32 v177, -v176, v51, v50
	v_cmp_lt_f32_e64 s[12:13], 0, v177
	s_nop 1
	v_cndmask_b32_e64 v51, v175, v176, s[12:13]
	v_div_scale_f32 v239, s[12:13], v51, v51, 1.0
	v_rcp_f32_e32 v240, v239
	s_nop 0
	v_fma_f32 v241, -v239, v240, 1.0
	v_fmac_f32_e32 v240, v241, v240
	v_div_scale_f32 v244, vcc, 1.0, v51, 1.0
	v_mul_f32_e32 v245, v244, v240
	v_fma_f32 v246, -v239, v245, v244
	v_fmac_f32_e32 v245, v246, v240
	v_fma_f32 v239, -v239, v245, v244
	v_div_fmas_f32 v239, v239, v240, v245
	v_div_fixup_f32 v51, v239, v51, 1.0
	v_mul_f32_e32 v220, v220, v51
	v_mul_f32_e32 v220, v52, v220
	v_mul_f32_e32 v221, v221, v51
	v_mul_f32_e32 v221, v53, v221
	v_mul_f32_e32 v222, v222, v51
	v_mul_f32_e32 v222, v54, v222
	v_mul_f32_e32 v223, v223, v51
	v_mul_f32_e32 v223, v55, v223
	v_mul_f32_e32 v224, v224, v51
	v_mul_f32_e32 v224, v56, v224
	v_mul_f32_e32 v225, v225, v51
	v_mul_f32_e32 v225, v57, v225
	v_mul_f32_e32 v226, v226, v51
	v_mul_f32_e32 v226, v58, v226
	v_mul_f32_e32 v227, v227, v51
	v_mul_f32_e32 v227, v59, v227
	v_mul_f32_e32 v228, v228, v51
	v_mul_f32_e32 v228, v60, v228
	v_mul_f32_e32 v229, v229, v51
	v_mul_f32_e32 v229, v61, v229
	v_mul_f32_e32 v230, v230, v51
	v_mul_f32_e32 v230, v62, v230
	v_mul_f32_e32 v231, v231, v51
	v_mul_f32_e32 v231, v63, v231
	v_mul_f32_e32 v232, v232, v51
	v_mul_f32_e32 v232, v64, v232
	v_mul_f32_e32 v233, v233, v51
	v_mul_f32_e32 v233, v65, v233
	v_mul_f32_e32 v234, v234, v51
	v_mul_f32_e32 v234, v66, v234
	v_mul_f32_e32 v235, v235, v51
	v_mul_f32_e32 v235, v67, v235
	v_cvt_pk_bf16_f32 v236, v220, v221
	v_cvt_pk_bf16_f32 v237, v222, v223
	v_cvt_pk_bf16_f32 v238, v224, v225
	v_cvt_pk_bf16_f32 v239, v226, v227
	v_cvt_pk_bf16_f32 v240, v228, v229
	v_cvt_pk_bf16_f32 v241, v230, v231
	v_cvt_pk_bf16_f32 v244, v232, v233
	v_cvt_pk_bf16_f32 v245, v234, v235
	v_mov_b32_e32 v220, v236
	v_mov_b32_e32 v221, v237
	v_mov_b32_e32 v222, v238
	v_mov_b32_e32 v223, v239
	v_mov_b32_e32 v224, v240
	v_mov_b32_e32 v225, v241
	v_mov_b32_e32 v226, v244
	v_mov_b32_e32 v227, v245
	global_store_dwordx4 v5, v[220:223], s[34:35]
	global_store_dwordx4 v5, v[224:227], s[34:35] offset:16
	v_add_u32_e32 v5, 0x800000, v5
	global_load_dwordx4 v[20:23], v1, s[34:35] nt
	global_load_dwordx4 v[24:27], v1, s[34:35] offset:16 nt
	v_add_u32_e32 v236, 0x2000000, v1
	global_load_dword v44, v2, s[34:35]
	global_load_dwordx4 v[28:31], v236, s[34:35] nt
	global_load_dwordx4 v[32:35], v236, s[34:35] offset:16 nt
	v_add_u32_e32 v237, 0x4000000, v1
	v_add_u32_e32 v238, 0x80000, v2
	global_load_dword v45, v238, s[34:35]
	global_load_dwordx4 v[36:39], v237, s[34:35] nt
	global_load_dwordx4 v[40:43], v237, s[34:35] offset:16 nt
	v_add_u32_e32 v238, 0x100000, v2
	global_load_dword v46, v238, s[34:35]
	v_add_u32_e32 v1, 0x400000, v1
	v_add_u32_e32 v2, 0x10000, v2
	s_waitcnt vmcnt(11)
	v_lshlrev_b32_e32 v220, 16, v148
	v_and_b32_e32 v221, 0xffff0000, v148
	v_lshlrev_b32_e32 v240, 16, v156
	v_and_b32_e32 v241, 0xffff0000, v156
	v_pk_add_f32 v[220:221], v[220:221], v[240:241]
	v_lshlrev_b32_e32 v240, 16, v164
	v_and_b32_e32 v241, 0xffff0000, v164
	v_pk_add_f32 v[220:221], v[220:221], v[240:241]
	v_lshlrev_b32_e32 v222, 16, v149
	v_and_b32_e32 v223, 0xffff0000, v149
	v_lshlrev_b32_e32 v240, 16, v157
	v_and_b32_e32 v241, 0xffff0000, v157
	v_pk_add_f32 v[222:223], v[222:223], v[240:241]
	v_lshlrev_b32_e32 v240, 16, v165
	v_and_b32_e32 v241, 0xffff0000, v165
	v_pk_add_f32 v[222:223], v[222:223], v[240:241]
	v_lshlrev_b32_e32 v224, 16, v150
	v_and_b32_e32 v225, 0xffff0000, v150
	v_lshlrev_b32_e32 v240, 16, v158
	v_and_b32_e32 v241, 0xffff0000, v158
	v_pk_add_f32 v[224:225], v[224:225], v[240:241]
	v_lshlrev_b32_e32 v240, 16, v166
	v_and_b32_e32 v241, 0xffff0000, v166
	v_pk_add_f32 v[224:225], v[224:225], v[240:241]
	v_lshlrev_b32_e32 v226, 16, v151
	v_and_b32_e32 v227, 0xffff0000, v151
	v_lshlrev_b32_e32 v240, 16, v159
	v_and_b32_e32 v241, 0xffff0000, v159
	v_pk_add_f32 v[226:227], v[226:227], v[240:241]
	v_lshlrev_b32_e32 v240, 16, v167
	v_and_b32_e32 v241, 0xffff0000, v167
	v_pk_add_f32 v[226:227], v[226:227], v[240:241]
	v_lshlrev_b32_e32 v228, 16, v152
	v_and_b32_e32 v229, 0xffff0000, v152
	v_lshlrev_b32_e32 v240, 16, v160
	v_and_b32_e32 v241, 0xffff0000, v160
	v_pk_add_f32 v[228:229], v[228:229], v[240:241]
	v_lshlrev_b32_e32 v240, 16, v168
	v_and_b32_e32 v241, 0xffff0000, v168
	v_pk_add_f32 v[228:229], v[228:229], v[240:241]
	v_lshlrev_b32_e32 v230, 16, v153
	v_and_b32_e32 v231, 0xffff0000, v153
	v_lshlrev_b32_e32 v240, 16, v161
	v_and_b32_e32 v241, 0xffff0000, v161
	v_pk_add_f32 v[230:231], v[230:231], v[240:241]
	v_lshlrev_b32_e32 v240, 16, v169
	v_and_b32_e32 v241, 0xffff0000, v169
	v_pk_add_f32 v[230:231], v[230:231], v[240:241]
	v_lshlrev_b32_e32 v232, 16, v154
	v_and_b32_e32 v233, 0xffff0000, v154
	v_lshlrev_b32_e32 v240, 16, v162
	v_and_b32_e32 v241, 0xffff0000, v162
	v_pk_add_f32 v[232:233], v[232:233], v[240:241]
	v_lshlrev_b32_e32 v240, 16, v170
	v_and_b32_e32 v241, 0xffff0000, v170
	v_pk_add_f32 v[232:233], v[232:233], v[240:241]
	v_lshlrev_b32_e32 v234, 16, v155
	v_and_b32_e32 v235, 0xffff0000, v155
	v_lshlrev_b32_e32 v240, 16, v163
	v_and_b32_e32 v241, 0xffff0000, v163
	v_pk_add_f32 v[234:235], v[234:235], v[240:241]
	v_lshlrev_b32_e32 v240, 16, v171
	v_and_b32_e32 v241, 0xffff0000, v171
	v_pk_add_f32 v[234:235], v[234:235], v[240:241]
	v_add_f32_e32 v247, v172, v173
	v_add_f32_e32 v247, v247, v174
	v_div_scale_f32 v239, s[12:13], v247, v247, 1.0
	v_rcp_f32_e32 v240, v239
	s_nop 0
	v_fma_f32 v241, -v239, v240, 1.0
	v_fmac_f32_e32 v240, v241, v240
	v_div_scale_f32 v244, vcc, 1.0, v247, 1.0
	v_mul_f32_e32 v245, v244, v240
	v_fma_f32 v246, -v239, v245, v244
	v_fmac_f32_e32 v245, v246, v240
	v_fma_f32 v239, -v239, v245, v244
	v_div_fmas_f32 v239, v239, v240, v245
	v_div_fixup_f32 v247, v239, v247, 1.0
	v_mul_f32_e32 v220, v247, v220
	v_mul_f32_e32 v221, v247, v221
	v_mul_f32_e32 v222, v247, v222
	v_mul_f32_e32 v223, v247, v223
	v_mul_f32_e32 v224, v247, v224
	v_mul_f32_e32 v225, v247, v225
	v_mul_f32_e32 v226, v247, v226
	v_mul_f32_e32 v227, v247, v227
	v_mul_f32_e32 v228, v247, v228
	v_mul_f32_e32 v229, v247, v229
	v_mul_f32_e32 v230, v247, v230
	v_mul_f32_e32 v231, v247, v231
	v_mul_f32_e32 v232, v247, v232
	v_mul_f32_e32 v233, v247, v233
	v_mul_f32_e32 v234, v247, v234
	v_mul_f32_e32 v235, v247, v235
	v_mul_f32_e32 v48, v220, v220
	v_fmac_f32_e32 v48, v221, v221
	v_mul_f32_e32 v49, v222, v222
	v_fmac_f32_e32 v49, v223, v223
	v_add_f32_e32 v48, v48, v49
	v_mov_b32_e32 v207, v48
	v_mul_f32_e32 v48, v224, v224
	v_fmac_f32_e32 v48, v225, v225
	v_mul_f32_e32 v49, v226, v226
	v_fmac_f32_e32 v49, v227, v227
	v_add_f32_e32 v48, v48, v49
	v_add_f32_e32 v207, v207, v48
	v_mul_f32_e32 v48, v228, v228
	v_fmac_f32_e32 v48, v229, v229
	v_mul_f32_e32 v49, v230, v230
	v_fmac_f32_e32 v49, v231, v231
	v_add_f32_e32 v48, v48, v49
	v_add_f32_e32 v207, v207, v48
	v_mul_f32_e32 v48, v232, v232
	v_fmac_f32_e32 v48, v233, v233
	v_mul_f32_e32 v49, v234, v234
	v_fmac_f32_e32 v49, v235, v235
	v_add_f32_e32 v48, v48, v49
	v_add_f32_e32 v207, v207, v48
	ds_swizzle_b32 v48, v207 offset:0x41f
	s_waitcnt lgkmcnt(0)
	v_add_f32_e32 v207, v207, v48
	ds_swizzle_b32 v48, v207 offset:0x81f
	s_waitcnt lgkmcnt(0)
	v_add_f32_e32 v207, v207, v48
	ds_swizzle_b32 v48, v207 offset:0x101f
	s_waitcnt lgkmcnt(0)
	v_add_f32_e32 v207, v207, v48
	v_fmamk_f32 v50, v207, 0x3c000000, v47
	v_sqrt_f32_e32 v51, v50
	s_nop 0
	v_add_u32_e32 v175, -1, v51
	v_fma_f32 v177, -v175, v51, v50
	v_cmp_ge_f32_e64 s[12:13], 0, v177
	v_add_u32_e32 v176, 1, v51
	s_nop 1
	v_cndmask_b32_e64 v175, v51, v175, s[12:13]
	v_fma_f32 v177, -v176, v51, v50
	v_cmp_lt_f32_e64 s[12:13], 0, v177
	s_nop 1
	v_cndmask_b32_e64 v51, v175, v176, s[12:13]
	v_div_scale_f32 v239, s[12:13], v51, v51, 1.0
	v_rcp_f32_e32 v240, v239
	s_nop 0
	v_fma_f32 v241, -v239, v240, 1.0
	v_fmac_f32_e32 v240, v241, v240
	v_div_scale_f32 v244, vcc, 1.0, v51, 1.0
	v_mul_f32_e32 v245, v244, v240
	v_fma_f32 v246, -v239, v245, v244
	v_fmac_f32_e32 v245, v246, v240
	v_fma_f32 v239, -v239, v245, v244
	v_div_fmas_f32 v239, v239, v240, v245
	v_div_fixup_f32 v51, v239, v51, 1.0
	v_mul_f32_e32 v220, v220, v51
	v_mul_f32_e32 v220, v52, v220
	v_mul_f32_e32 v221, v221, v51
	v_mul_f32_e32 v221, v53, v221
	v_mul_f32_e32 v222, v222, v51
	v_mul_f32_e32 v222, v54, v222
	v_mul_f32_e32 v223, v223, v51
	v_mul_f32_e32 v223, v55, v223
	v_mul_f32_e32 v224, v224, v51
	v_mul_f32_e32 v224, v56, v224
	v_mul_f32_e32 v225, v225, v51
	v_mul_f32_e32 v225, v57, v225
	v_mul_f32_e32 v226, v226, v51
	v_mul_f32_e32 v226, v58, v226
	v_mul_f32_e32 v227, v227, v51
	v_mul_f32_e32 v227, v59, v227
	v_mul_f32_e32 v228, v228, v51
	v_mul_f32_e32 v228, v60, v228
	v_mul_f32_e32 v229, v229, v51
	v_mul_f32_e32 v229, v61, v229
	v_mul_f32_e32 v230, v230, v51
	v_mul_f32_e32 v230, v62, v230
	v_mul_f32_e32 v231, v231, v51
	v_mul_f32_e32 v231, v63, v231
	v_mul_f32_e32 v232, v232, v51
	v_mul_f32_e32 v232, v64, v232
	v_mul_f32_e32 v233, v233, v51
	v_mul_f32_e32 v233, v65, v233
	v_mul_f32_e32 v234, v234, v51
	v_mul_f32_e32 v234, v66, v234
	v_mul_f32_e32 v235, v235, v51
	v_mul_f32_e32 v235, v67, v235
	v_cvt_pk_bf16_f32 v236, v220, v221
	v_cvt_pk_bf16_f32 v237, v222, v223
	v_cvt_pk_bf16_f32 v238, v224, v225
	v_cvt_pk_bf16_f32 v239, v226, v227
	v_cvt_pk_bf16_f32 v240, v228, v229
	v_cvt_pk_bf16_f32 v241, v230, v231
	v_cvt_pk_bf16_f32 v244, v232, v233
	v_cvt_pk_bf16_f32 v245, v234, v235
	v_mov_b32_e32 v220, v236
	v_mov_b32_e32 v221, v237
	v_mov_b32_e32 v222, v238
	v_mov_b32_e32 v223, v239
	v_mov_b32_e32 v224, v240
	v_mov_b32_e32 v225, v241
	v_mov_b32_e32 v226, v244
	v_mov_b32_e32 v227, v245
	global_store_dwordx4 v5, v[220:223], s[34:35]
	global_store_dwordx4 v5, v[224:227], s[34:35] offset:16
	v_add_u32_e32 v5, 0x800000, v5
	global_load_dwordx4 v[148:151], v1, s[34:35] nt
	global_load_dwordx4 v[152:155], v1, s[34:35] offset:16 nt
	v_add_u32_e32 v236, 0x2000000, v1
	global_load_dword v172, v2, s[34:35]
	global_load_dwordx4 v[156:159], v236, s[34:35] nt
	global_load_dwordx4 v[160:163], v236, s[34:35] offset:16 nt
	v_add_u32_e32 v237, 0x4000000, v1
	v_add_u32_e32 v238, 0x80000, v2
	global_load_dword v173, v238, s[34:35]
	global_load_dwordx4 v[164:167], v237, s[34:35] nt
	global_load_dwordx4 v[168:171], v237, s[34:35] offset:16 nt
	v_add_u32_e32 v238, 0x100000, v2
	global_load_dword v174, v238, s[34:35]
	v_add_u32_e32 v1, 0x400000, v1
	v_add_u32_e32 v2, 0x10000, v2
	s_add_i32 s8, s8, 1
	s_cmp_lt_u32 s8, 4
	s_cbranch_scc1 .Lcb_loop
	s_waitcnt vmcnt(0)
